# code placement: the 18 GEMM K-loop heads aligned to 64 B (.p2align 6) on top of early-invalidate barrier
# speedup vs baseline: 1.0075x; 1.0072x over previous
;     ...
;         for (int a = 0; a < 2; ++a)
; #pragma unroll
;             for (int b = 0; b < 2; ++b)
; #pragma unroll
;                 for (int m = 0; m < 4; ++m)
; #pragma unroll
;                     for (int n = 0; n < 2; ++n) acc[a][b][m][n] = (f32x4){0.f, 0.f, 0.f, 0.f};
;         cur = nxt; cA = nA; cB = nB; ++ui;
.LBB0_189:
	s_ashr_i32 s17, s16, 31
	s_lshl_b64 s[20:21], s[16:17], 19
	s_cmpk_gt_i32 s14, 0x3e7
	s_cselect_b32 s15, s28, s30
	s_cselect_b32 s0, s29, s31
	s_add_u32 s20, s15, s20
	s_addc_u32 s21, s0, s21
	s_and_b64 s[26:27], s[26:27], exec
	s_cselect_b32 s0, s21, s25
	s_cselect_b32 s15, s20, s24
	s_add_u32 s22, s22, 0x40080
	s_addc_u32 s23, s23, 0
	s_add_u32 s17, s24, 0x100
	v_mov_b32_e32 v2, 0
	s_addc_u32 s45, s25, 0
	s_mov_b32 s46, -2
	v_mov_b32_e32 v3, v2
	v_mov_b64_e32 v[4:5], v[2:3]
	v_mov_b64_e32 v[6:7], v[2:3]
	v_mov_b64_e32 v[8:9], v[2:3]
	v_mov_b64_e32 v[10:11], v[2:3]
	v_mov_b64_e32 v[12:13], v[2:3]
	v_mov_b64_e32 v[14:15], v[2:3]
	v_mov_b64_e32 v[16:17], v[2:3]
	v_mov_b64_e32 v[18:19], v[2:3]
	v_mov_b64_e32 v[20:21], v[2:3]
	v_mov_b64_e32 v[22:23], v[2:3]
	v_mov_b64_e32 v[24:25], v[2:3]
	v_mov_b64_e32 v[26:27], v[2:3]
	v_mov_b64_e32 v[28:29], v[2:3]
	v_mov_b64_e32 v[30:31], v[2:3]
	v_mov_b64_e32 v[32:33], v[2:3]
	v_mov_b64_e32 v[34:35], v[2:3]
	v_mov_b64_e32 v[36:37], v[2:3]
	v_mov_b64_e32 v[38:39], v[2:3]
	v_mov_b64_e32 v[40:41], v[2:3]
	v_mov_b64_e32 v[42:43], v[2:3]
	v_mov_b64_e32 v[44:45], v[2:3]
	v_mov_b64_e32 v[46:47], v[2:3]
	v_mov_b64_e32 v[48:49], v[2:3]
	v_mov_b64_e32 v[50:51], v[2:3]
	v_mov_b64_e32 v[52:53], v[2:3]
	v_mov_b64_e32 v[54:55], v[2:3]
	v_mov_b64_e32 v[56:57], v[2:3]
	v_mov_b64_e32 v[58:59], v[2:3]
	v_mov_b64_e32 v[60:61], v[2:3]
	v_mov_b64_e32 v[62:63], v[2:3]
	v_mov_b64_e32 v[64:65], v[2:3]
	v_mov_b64_e32 v[66:67], v[2:3]
	v_mov_b64_e32 v[68:69], v[2:3]
	v_mov_b64_e32 v[70:71], v[2:3]
	v_mov_b64_e32 v[72:73], v[2:3]
	v_mov_b64_e32 v[74:75], v[2:3]
	v_mov_b64_e32 v[76:77], v[2:3]
	v_mov_b64_e32 v[78:79], v[2:3]
	v_mov_b64_e32 v[80:81], v[2:3]
	v_mov_b64_e32 v[82:83], v[2:3]
	v_mov_b64_e32 v[84:85], v[2:3]
	v_mov_b64_e32 v[86:87], v[2:3]
	v_mov_b64_e32 v[88:89], v[2:3]
	v_mov_b64_e32 v[90:91], v[2:3]
	v_mov_b64_e32 v[92:93], v[2:3]
	v_mov_b64_e32 v[94:95], v[2:3]
	v_mov_b64_e32 v[96:97], v[2:3]
	v_mov_b64_e32 v[98:99], v[2:3]
	v_mov_b64_e32 v[100:101], v[2:3]
	v_mov_b64_e32 v[102:103], v[2:3]
	v_mov_b64_e32 v[104:105], v[2:3]
	v_mov_b64_e32 v[106:107], v[2:3]
	v_mov_b64_e32 v[108:109], v[2:3]
	v_mov_b64_e32 v[110:111], v[2:3]
	v_mov_b64_e32 v[112:113], v[2:3]
	v_mov_b64_e32 v[114:115], v[2:3]
	v_mov_b64_e32 v[116:117], v[2:3]
	v_mov_b64_e32 v[118:119], v[2:3]
	v_mov_b64_e32 v[120:121], v[2:3]
	v_mov_b64_e32 v[122:123], v[2:3]
	v_mov_b64_e32 v[124:125], v[2:3]
	v_mov_b64_e32 v[126:127], v[2:3]
	v_mov_b64_e32 v[128:129], v[2:3]
	.p2align	6

;     __device__ __forceinline__ bool next(int i, Unit& u) const { return unit_of((long)i * G + c, u); }
;     __device__ __forceinline__ bool next(int i, Unit& u) const { if (i >= 64) return false; return unit_of((long)__builtin_amdgcn_readfirstlane(list[i]), u); }
;     ...
;         const bool has_next = S.next(ui + 1, nxt);
;         const char* nA = has_next ? S.a_base(nxt) : cA; const char* nB = has_next ? S.b_base(nxt) : cB;
;         for (int t = 0; t < nt; t += 2) {
;             const bool last = (t == nt - 2);
;             const char* a1 = cA + (size_t)(t + 1) * kstep;
;             const char* a2 = last ? nA : cA + (size_t)(t + 2) * kstep; const char* b2 = last ? nB : cB + (size_t)(t + 2) * kstep;
;             const char* a3 = a2 + kstep; const char* b3 = b2 + kstep;
;     ...
;         for (int a = 0; a < 2; ++a)
; #pragma unroll
;             for (int b = 0; b < 2; ++b)
; #pragma unroll
;                 for (int m = 0; m < 4; ++m)
; #pragma unroll
;                     for (int n = 0; n < 2; ++n) acc[a][b][m][n] = (f32x4){0.f, 0.f, 0.f, 0.f};
;         cur = nxt; cA = nA; cB = nB; ++ui;
.LBB0_840:
	s_ashr_i32 s11, s10, 31
	s_lshl_b64 s[12:13], s[10:11], 19
	s_add_u32 s12, s24, s12
	s_addc_u32 s13, s25, s13
	s_and_b64 s[14:15], s[4:5], exec
	s_cselect_b32 s11, s13, s19
	s_cselect_b32 s17, s12, s18
	s_ashr_i32 s9, s8, 31
	s_lshl_b64 s[14:15], s[8:9], 19
	s_add_u32 s14, s26, s14
	s_addc_u32 s15, s27, s15
	s_and_b64 s[22:23], s[4:5], exec
	s_cselect_b32 s9, s15, s21
	s_cselect_b32 s47, s14, s20
	s_add_u32 s18, s18, 0x40080
	s_addc_u32 s19, s19, 0
	s_add_u32 s48, s20, 0x100
	v_mov_b32_e32 v2, 0
	s_addc_u32 s49, s21, 0
	s_mov_b32 s50, -2
	v_mov_b32_e32 v3, v2
	v_mov_b64_e32 v[4:5], v[2:3]
	v_mov_b64_e32 v[6:7], v[2:3]
	v_mov_b64_e32 v[8:9], v[2:3]
	v_mov_b64_e32 v[10:11], v[2:3]
	v_mov_b64_e32 v[12:13], v[2:3]
	v_mov_b64_e32 v[14:15], v[2:3]
	v_mov_b64_e32 v[16:17], v[2:3]
	v_mov_b64_e32 v[18:19], v[2:3]
	v_mov_b64_e32 v[20:21], v[2:3]
	v_mov_b64_e32 v[22:23], v[2:3]
	v_mov_b64_e32 v[24:25], v[2:3]
	v_mov_b64_e32 v[26:27], v[2:3]
	v_mov_b64_e32 v[28:29], v[2:3]
	v_mov_b64_e32 v[30:31], v[2:3]
	v_mov_b64_e32 v[32:33], v[2:3]
	v_mov_b64_e32 v[34:35], v[2:3]
	v_mov_b64_e32 v[36:37], v[2:3]
	v_mov_b64_e32 v[38:39], v[2:3]
	v_mov_b64_e32 v[40:41], v[2:3]
	v_mov_b64_e32 v[42:43], v[2:3]
	v_mov_b64_e32 v[44:45], v[2:3]
	v_mov_b64_e32 v[46:47], v[2:3]
	v_mov_b64_e32 v[48:49], v[2:3]
	v_mov_b64_e32 v[50:51], v[2:3]
	v_mov_b64_e32 v[52:53], v[2:3]
	v_mov_b64_e32 v[54:55], v[2:3]
	v_mov_b64_e32 v[56:57], v[2:3]
	v_mov_b64_e32 v[58:59], v[2:3]
	v_mov_b64_e32 v[60:61], v[2:3]
	v_mov_b64_e32 v[62:63], v[2:3]
	v_mov_b64_e32 v[64:65], v[2:3]
	v_mov_b64_e32 v[66:67], v[2:3]
	v_mov_b64_e32 v[68:69], v[2:3]
	v_mov_b64_e32 v[70:71], v[2:3]
	v_mov_b64_e32 v[72:73], v[2:3]
	v_mov_b64_e32 v[74:75], v[2:3]
	v_mov_b64_e32 v[76:77], v[2:3]
	v_mov_b64_e32 v[78:79], v[2:3]
	v_mov_b64_e32 v[80:81], v[2:3]
	v_mov_b64_e32 v[82:83], v[2:3]
	v_mov_b64_e32 v[84:85], v[2:3]
	v_mov_b64_e32 v[86:87], v[2:3]
	v_mov_b64_e32 v[88:89], v[2:3]
	v_mov_b64_e32 v[90:91], v[2:3]
	v_mov_b64_e32 v[92:93], v[2:3]
	v_mov_b64_e32 v[94:95], v[2:3]
	v_mov_b64_e32 v[96:97], v[2:3]
	v_mov_b64_e32 v[98:99], v[2:3]
	v_mov_b64_e32 v[100:101], v[2:3]
	v_mov_b64_e32 v[102:103], v[2:3]
	v_mov_b64_e32 v[104:105], v[2:3]
	v_mov_b64_e32 v[106:107], v[2:3]
	v_mov_b64_e32 v[108:109], v[2:3]
	v_mov_b64_e32 v[110:111], v[2:3]
	v_mov_b64_e32 v[112:113], v[2:3]
	v_mov_b64_e32 v[114:115], v[2:3]
	v_mov_b64_e32 v[116:117], v[2:3]
	v_mov_b64_e32 v[118:119], v[2:3]
	v_mov_b64_e32 v[120:121], v[2:3]
	v_mov_b64_e32 v[122:123], v[2:3]
	v_mov_b64_e32 v[124:125], v[2:3]
	v_mov_b64_e32 v[126:127], v[2:3]
	v_mov_b64_e32 v[128:129], v[2:3]
	.p2align	6

;     __device__ __forceinline__ bool next(int i, Unit& u) const { return unit_of((long)i * G + c, u); }
;     __device__ __forceinline__ bool next(int i, Unit& u) const { if (i >= 64) return false; return unit_of((long)__builtin_amdgcn_readfirstlane(list[i]), u); }
;     ...
;         const bool has_next = S.next(ui + 1, nxt);
;         const char* nA = has_next ? S.a_base(nxt) : cA; const char* nB = has_next ? S.b_base(nxt) : cB;
;         for (int t = 0; t < nt; t += 2) {
;             const bool last = (t == nt - 2);
;             const char* a1 = cA + (size_t)(t + 1) * kstep;
;             const char* a2 = last ? nA : cA + (size_t)(t + 2) * kstep; const char* b2 = last ? nB : cB + (size_t)(t + 2) * kstep;
;             const char* a3 = a2 + kstep; const char* b3 = b2 + kstep;
;     ...
;         for (int a = 0; a < 2; ++a)
; #pragma unroll
;             for (int b = 0; b < 2; ++b)
; #pragma unroll
;                 for (int m = 0; m < 4; ++m)
; #pragma unroll
;                     for (int n = 0; n < 2; ++n) acc[a][b][m][n] = (f32x4){0.f, 0.f, 0.f, 0.f};
;         cur = nxt; cA = nA; cB = nB; ++ui;
.LBB0_994:
	s_ashr_i32 s13, s12, 31
	s_lshl_b64 s[14:15], s[12:13], 19
	s_add_u32 s14, s26, s14
	s_addc_u32 s15, s27, s15
	s_and_b64 s[16:17], s[4:5], exec
	s_cselect_b32 s13, s15, s21
	s_cselect_b32 s49, s14, s20
	s_ashr_i32 s11, s10, 31
	s_lshl_b64 s[16:17], s[10:11], 19
	s_add_u32 s16, s28, s16
	s_addc_u32 s17, s29, s17
	s_and_b64 s[24:25], s[4:5], exec
	s_cselect_b32 s11, s17, s23
	s_cselect_b32 s50, s16, s22
	s_add_u32 s20, s20, 0x40080
	s_addc_u32 s21, s21, 0
	s_add_u32 s51, s22, 0x100
	v_mov_b32_e32 v2, 0
	s_addc_u32 s52, s23, 0
	s_mov_b32 s53, -2
	v_mov_b32_e32 v3, v2
	v_mov_b64_e32 v[4:5], v[2:3]
	v_mov_b64_e32 v[6:7], v[2:3]
	v_mov_b64_e32 v[8:9], v[2:3]
	v_mov_b64_e32 v[10:11], v[2:3]
	v_mov_b64_e32 v[12:13], v[2:3]
	v_mov_b64_e32 v[14:15], v[2:3]
	v_mov_b64_e32 v[16:17], v[2:3]
	v_mov_b64_e32 v[18:19], v[2:3]
	v_mov_b64_e32 v[20:21], v[2:3]
	v_mov_b64_e32 v[22:23], v[2:3]
	v_mov_b64_e32 v[24:25], v[2:3]
	v_mov_b64_e32 v[26:27], v[2:3]
	v_mov_b64_e32 v[28:29], v[2:3]
	v_mov_b64_e32 v[30:31], v[2:3]
	v_mov_b64_e32 v[32:33], v[2:3]
	v_mov_b64_e32 v[34:35], v[2:3]
	v_mov_b64_e32 v[36:37], v[2:3]
	v_mov_b64_e32 v[38:39], v[2:3]
	v_mov_b64_e32 v[40:41], v[2:3]
	v_mov_b64_e32 v[42:43], v[2:3]
	v_mov_b64_e32 v[44:45], v[2:3]
	v_mov_b64_e32 v[46:47], v[2:3]
	v_mov_b64_e32 v[48:49], v[2:3]
	v_mov_b64_e32 v[50:51], v[2:3]
	v_mov_b64_e32 v[52:53], v[2:3]
	v_mov_b64_e32 v[54:55], v[2:3]
	v_mov_b64_e32 v[56:57], v[2:3]
	v_mov_b64_e32 v[58:59], v[2:3]
	v_mov_b64_e32 v[60:61], v[2:3]
	v_mov_b64_e32 v[62:63], v[2:3]
	v_mov_b64_e32 v[64:65], v[2:3]
	v_mov_b64_e32 v[66:67], v[2:3]
	v_mov_b64_e32 v[68:69], v[2:3]
	v_mov_b64_e32 v[70:71], v[2:3]
	v_mov_b64_e32 v[72:73], v[2:3]
	v_mov_b64_e32 v[74:75], v[2:3]
	v_mov_b64_e32 v[76:77], v[2:3]
	v_mov_b64_e32 v[78:79], v[2:3]
	v_mov_b64_e32 v[80:81], v[2:3]
	v_mov_b64_e32 v[82:83], v[2:3]
	v_mov_b64_e32 v[84:85], v[2:3]
	v_mov_b64_e32 v[86:87], v[2:3]
	v_mov_b64_e32 v[88:89], v[2:3]
	v_mov_b64_e32 v[90:91], v[2:3]
	v_mov_b64_e32 v[92:93], v[2:3]
	v_mov_b64_e32 v[94:95], v[2:3]
	v_mov_b64_e32 v[96:97], v[2:3]
	v_mov_b64_e32 v[98:99], v[2:3]
	v_mov_b64_e32 v[100:101], v[2:3]
	v_mov_b64_e32 v[102:103], v[2:3]
	v_mov_b64_e32 v[104:105], v[2:3]
	v_mov_b64_e32 v[106:107], v[2:3]
	v_mov_b64_e32 v[108:109], v[2:3]
	v_mov_b64_e32 v[110:111], v[2:3]
	v_mov_b64_e32 v[112:113], v[2:3]
	v_mov_b64_e32 v[114:115], v[2:3]
	v_mov_b64_e32 v[116:117], v[2:3]
	v_mov_b64_e32 v[118:119], v[2:3]
	v_mov_b64_e32 v[120:121], v[2:3]
	v_mov_b64_e32 v[122:123], v[2:3]
	v_mov_b64_e32 v[124:125], v[2:3]
	v_mov_b64_e32 v[126:127], v[2:3]
	v_mov_b64_e32 v[128:129], v[2:3]
	.p2align	6

;     ...
;             const char* a1 = cA + (size_t)(t + 1) * kstep;
;             const char* a2 = last ? nA : cA + (size_t)(t + 2) * kstep; const char* b2 = last ? nB : cB + (size_t)(t + 2) * kstep;
;             const char* a3 = a2 + kstep; const char* b3 = b2 + kstep;
;     ...
;         for (int a = 0; a < 2; ++a)
; #pragma unroll
;             for (int b = 0; b < 2; ++b)
; #pragma unroll
;                 for (int m = 0; m < 4; ++m)
; #pragma unroll
;                     for (int n = 0; n < 2; ++n) acc[a][b][m][n] = (f32x4){0.f, 0.f, 0.f, 0.f};
;         cur = nxt; cA = nA; cB = nB; ++ui;
.LBB0_1088:
	s_add_u32 s14, s14, 0xb0080
	s_addc_u32 s15, s15, 0
	s_add_u32 s13, s16, 0x100
	v_mov_b32_e32 v2, 0
	s_addc_u32 s46, s17, 0
	s_mov_b32 s47, -2
	v_mov_b32_e32 v3, v2
	v_mov_b32_e32 v4, v2
	v_mov_b32_e32 v5, v2
	v_mov_b32_e32 v6, v2
	v_mov_b32_e32 v7, v2
	v_mov_b32_e32 v8, v2
	v_mov_b32_e32 v9, v2
	v_mov_b32_e32 v14, v2
	v_mov_b32_e32 v15, v2
	v_mov_b32_e32 v16, v2
	v_mov_b32_e32 v17, v2
	v_mov_b32_e32 v22, v2
	v_mov_b32_e32 v23, v2
	v_mov_b32_e32 v24, v2
	v_mov_b32_e32 v25, v2
	v_mov_b32_e32 v30, v2
	v_mov_b32_e32 v31, v2
	v_mov_b32_e32 v32, v2
	v_mov_b32_e32 v33, v2
	v_mov_b32_e32 v38, v2
	v_mov_b32_e32 v39, v2
	v_mov_b32_e32 v40, v2
	v_mov_b32_e32 v41, v2
	v_mov_b32_e32 v46, v2
	v_mov_b32_e32 v47, v2
	v_mov_b32_e32 v48, v2
	v_mov_b32_e32 v49, v2
	v_mov_b32_e32 v54, v2
	v_mov_b32_e32 v55, v2
	v_mov_b32_e32 v56, v2
	v_mov_b32_e32 v57, v2
	v_mov_b32_e32 v10, v2
	v_mov_b32_e32 v11, v2
	v_mov_b32_e32 v12, v2
	v_mov_b32_e32 v13, v2
	v_mov_b32_e32 v18, v2
	v_mov_b32_e32 v19, v2
	v_mov_b32_e32 v20, v2
	v_mov_b32_e32 v21, v2
	v_mov_b32_e32 v26, v2
	v_mov_b32_e32 v27, v2
	v_mov_b32_e32 v28, v2
	v_mov_b32_e32 v29, v2
	v_mov_b32_e32 v34, v2
	v_mov_b32_e32 v35, v2
	v_mov_b32_e32 v36, v2
	v_mov_b32_e32 v37, v2
	v_mov_b32_e32 v42, v2
	v_mov_b32_e32 v43, v2
	v_mov_b32_e32 v44, v2
	v_mov_b32_e32 v45, v2
	v_mov_b32_e32 v50, v2
	v_mov_b32_e32 v51, v2
	v_mov_b32_e32 v52, v2
	v_mov_b32_e32 v53, v2
	v_mov_b32_e32 v58, v2
	v_mov_b32_e32 v59, v2
	v_mov_b32_e32 v60, v2
	v_mov_b32_e32 v61, v2
	v_mov_b32_e32 v62, v2
	v_mov_b32_e32 v63, v2
	v_mov_b32_e32 v64, v2
	v_mov_b32_e32 v65, v2
	v_mov_b32_e32 v66, v2
	v_mov_b32_e32 v67, v2
	v_mov_b32_e32 v68, v2
	v_mov_b32_e32 v69, v2
	v_mov_b32_e32 v70, v2
	v_mov_b32_e32 v71, v2
	v_mov_b32_e32 v72, v2
	v_mov_b32_e32 v73, v2
	v_mov_b32_e32 v78, v2
	v_mov_b32_e32 v79, v2
	v_mov_b32_e32 v80, v2
	v_mov_b32_e32 v81, v2
	v_mov_b32_e32 v86, v2
	v_mov_b32_e32 v87, v2
	v_mov_b32_e32 v88, v2
	v_mov_b32_e32 v89, v2
	v_mov_b32_e32 v94, v2
	v_mov_b32_e32 v95, v2
	v_mov_b32_e32 v96, v2
	v_mov_b32_e32 v97, v2
	v_mov_b32_e32 v102, v2
	v_mov_b32_e32 v103, v2
	v_mov_b32_e32 v104, v2
	v_mov_b32_e32 v105, v2
	v_mov_b32_e32 v130, v2
	v_mov_b32_e32 v131, v2
	v_mov_b32_e32 v132, v2
	v_mov_b32_e32 v133, v2
	v_mov_b32_e32 v134, v2
	v_mov_b32_e32 v135, v2
	v_mov_b32_e32 v136, v2
	v_mov_b32_e32 v137, v2
	v_mov_b32_e32 v74, v2
	v_mov_b32_e32 v75, v2
	v_mov_b32_e32 v76, v2
	v_mov_b32_e32 v77, v2
	v_mov_b32_e32 v82, v2
	v_mov_b32_e32 v83, v2
	v_mov_b32_e32 v84, v2
	v_mov_b32_e32 v85, v2
	v_mov_b32_e32 v90, v2
	v_mov_b32_e32 v91, v2
	v_mov_b32_e32 v92, v2
	v_mov_b32_e32 v93, v2
	v_mov_b32_e32 v98, v2
	v_mov_b32_e32 v99, v2
	v_mov_b32_e32 v100, v2
	v_mov_b32_e32 v101, v2
	v_mov_b32_e32 v106, v2
	v_mov_b32_e32 v107, v2
	v_mov_b32_e32 v108, v2
	v_mov_b32_e32 v109, v2
	v_mov_b32_e32 v110, v2
	v_mov_b32_e32 v111, v2
	v_mov_b32_e32 v112, v2
	v_mov_b32_e32 v113, v2
	v_mov_b32_e32 v138, v2
	v_mov_b32_e32 v139, v2
	v_mov_b32_e32 v140, v2
	v_mov_b32_e32 v141, v2
	v_mov_b32_e32 v142, v2
	v_mov_b32_e32 v143, v2
	v_mov_b32_e32 v144, v2
	v_mov_b32_e32 v145, v2
	.p2align	6

;     ...
;             const char* a1 = cA + (size_t)(t + 1) * kstep;
;             const char* a2 = last ? nA : cA + (size_t)(t + 2) * kstep; const char* b2 = last ? nB : cB + (size_t)(t + 2) * kstep;
;             const char* a3 = a2 + kstep; const char* b3 = b2 + kstep;
;     ...
;         for (int a = 0; a < 2; ++a)
; #pragma unroll
;             for (int b = 0; b < 2; ++b)
; #pragma unroll
;                 for (int m = 0; m < 4; ++m)
; #pragma unroll
;                     for (int n = 0; n < 2; ++n) acc[a][b][m][n] = (f32x4){0.f, 0.f, 0.f, 0.f};
;         cur = nxt; cA = nA; cB = nB; ++ui;
.LBB0_1116:
	s_add_u32 s14, s14, 0xb0080
	s_addc_u32 s15, s15, 0
	s_add_u32 s0, s16, 0x100
	v_mov_b32_e32 v2, 0
	s_addc_u32 s47, s17, 0
	s_mov_b32 s48, -2
	v_mov_b32_e32 v3, v2
	v_mov_b64_e32 v[4:5], v[2:3]
	v_mov_b64_e32 v[6:7], v[2:3]
	v_mov_b64_e32 v[8:9], v[2:3]
	v_mov_b64_e32 v[10:11], v[2:3]
	v_mov_b64_e32 v[12:13], v[2:3]
	v_mov_b64_e32 v[14:15], v[2:3]
	v_mov_b64_e32 v[16:17], v[2:3]
	v_mov_b64_e32 v[18:19], v[2:3]
	v_mov_b64_e32 v[20:21], v[2:3]
	v_mov_b64_e32 v[22:23], v[2:3]
	v_mov_b64_e32 v[24:25], v[2:3]
	v_mov_b64_e32 v[26:27], v[2:3]
	v_mov_b64_e32 v[28:29], v[2:3]
	v_mov_b64_e32 v[30:31], v[2:3]
	v_mov_b64_e32 v[32:33], v[2:3]
	v_mov_b64_e32 v[34:35], v[2:3]
	v_mov_b64_e32 v[36:37], v[2:3]
	v_mov_b64_e32 v[38:39], v[2:3]
	v_mov_b64_e32 v[40:41], v[2:3]
	v_mov_b64_e32 v[42:43], v[2:3]
	v_mov_b64_e32 v[44:45], v[2:3]
	v_mov_b64_e32 v[46:47], v[2:3]
	v_mov_b64_e32 v[48:49], v[2:3]
	v_mov_b64_e32 v[50:51], v[2:3]
	v_mov_b64_e32 v[52:53], v[2:3]
	v_mov_b64_e32 v[54:55], v[2:3]
	v_mov_b64_e32 v[56:57], v[2:3]
	v_mov_b64_e32 v[58:59], v[2:3]
	v_mov_b64_e32 v[60:61], v[2:3]
	v_mov_b64_e32 v[62:63], v[2:3]
	v_mov_b64_e32 v[64:65], v[2:3]
	v_mov_b64_e32 v[66:67], v[2:3]
	v_mov_b64_e32 v[68:69], v[2:3]
	v_mov_b64_e32 v[70:71], v[2:3]
	v_mov_b64_e32 v[72:73], v[2:3]
	v_mov_b64_e32 v[74:75], v[2:3]
	v_mov_b64_e32 v[76:77], v[2:3]
	v_mov_b64_e32 v[78:79], v[2:3]
	v_mov_b64_e32 v[80:81], v[2:3]
	v_mov_b64_e32 v[82:83], v[2:3]
	v_mov_b64_e32 v[84:85], v[2:3]
	v_mov_b64_e32 v[86:87], v[2:3]
	v_mov_b64_e32 v[88:89], v[2:3]
	v_mov_b64_e32 v[90:91], v[2:3]
	v_mov_b64_e32 v[92:93], v[2:3]
	v_mov_b64_e32 v[94:95], v[2:3]
	v_mov_b64_e32 v[96:97], v[2:3]
	v_mov_b64_e32 v[98:99], v[2:3]
	v_mov_b64_e32 v[100:101], v[2:3]
	v_mov_b64_e32 v[102:103], v[2:3]
	v_mov_b64_e32 v[104:105], v[2:3]
	v_mov_b64_e32 v[106:107], v[2:3]
	v_mov_b64_e32 v[108:109], v[2:3]
	v_mov_b64_e32 v[110:111], v[2:3]
	v_mov_b64_e32 v[112:113], v[2:3]
	v_mov_b64_e32 v[114:115], v[2:3]
	v_mov_b64_e32 v[116:117], v[2:3]
	v_mov_b64_e32 v[118:119], v[2:3]
	v_mov_b64_e32 v[120:121], v[2:3]
	v_mov_b64_e32 v[122:123], v[2:3]
	v_mov_b64_e32 v[124:125], v[2:3]
	v_mov_b64_e32 v[126:127], v[2:3]
	v_mov_b64_e32 v[128:129], v[2:3]
	.p2align	6

;     ...
;             const char* a1 = cA + (size_t)(t + 1) * kstep;
;             const char* a2 = last ? nA : cA + (size_t)(t + 2) * kstep; const char* b2 = last ? nB : cB + (size_t)(t + 2) * kstep;
;             const char* a3 = a2 + kstep; const char* b3 = b2 + kstep;
;     ...
;         for (int a = 0; a < 2; ++a)
; #pragma unroll
;             for (int b = 0; b < 2; ++b)
; #pragma unroll
;                 for (int m = 0; m < 4; ++m)
; #pragma unroll
;                     for (int n = 0; n < 2; ++n) acc[a][b][m][n] = (f32x4){0.f, 0.f, 0.f, 0.f};
;         cur = nxt; cA = nA; cB = nB; ++ui;
.LBB0_2241:
	s_add_u32 s74, s74, 0xe0080
	v_lshl_add_u64 v[164:165], v[2:3], 0, s[88:89]
	v_mov_b32_e32 v2, 0
	s_addc_u32 s75, s75, 0
	s_mov_b32 s19, -2
	v_mov_b32_e32 v3, v2
	v_mov_b64_e32 v[4:5], v[2:3]
	v_mov_b64_e32 v[6:7], v[2:3]
	v_mov_b64_e32 v[8:9], v[2:3]
	v_mov_b64_e32 v[10:11], v[2:3]
	v_mov_b64_e32 v[12:13], v[2:3]
	v_mov_b64_e32 v[14:15], v[2:3]
	v_mov_b64_e32 v[16:17], v[2:3]
	v_mov_b64_e32 v[18:19], v[2:3]
	v_mov_b64_e32 v[20:21], v[2:3]
	v_mov_b64_e32 v[22:23], v[2:3]
	v_mov_b64_e32 v[24:25], v[2:3]
	v_mov_b64_e32 v[26:27], v[2:3]
	v_mov_b64_e32 v[28:29], v[2:3]
	v_mov_b64_e32 v[30:31], v[2:3]
	v_mov_b64_e32 v[32:33], v[2:3]
	v_mov_b64_e32 v[34:35], v[2:3]
	v_mov_b64_e32 v[36:37], v[2:3]
	v_mov_b64_e32 v[38:39], v[2:3]
	v_mov_b64_e32 v[40:41], v[2:3]
	v_mov_b64_e32 v[42:43], v[2:3]
	v_mov_b64_e32 v[44:45], v[2:3]
	v_mov_b64_e32 v[46:47], v[2:3]
	v_mov_b64_e32 v[48:49], v[2:3]
	v_mov_b64_e32 v[50:51], v[2:3]
	v_mov_b64_e32 v[52:53], v[2:3]
	v_mov_b64_e32 v[54:55], v[2:3]
	v_mov_b64_e32 v[56:57], v[2:3]
	v_mov_b64_e32 v[58:59], v[2:3]
	v_mov_b64_e32 v[60:61], v[2:3]
	v_mov_b64_e32 v[62:63], v[2:3]
	v_mov_b64_e32 v[64:65], v[2:3]
	v_mov_b64_e32 v[66:67], v[2:3]
	v_mov_b64_e32 v[68:69], v[2:3]
	v_mov_b64_e32 v[70:71], v[2:3]
	v_mov_b64_e32 v[72:73], v[2:3]
	v_mov_b64_e32 v[74:75], v[2:3]
	v_mov_b64_e32 v[76:77], v[2:3]
	v_mov_b64_e32 v[78:79], v[2:3]
	v_mov_b64_e32 v[80:81], v[2:3]
	v_mov_b64_e32 v[82:83], v[2:3]
	v_mov_b64_e32 v[84:85], v[2:3]
	v_mov_b64_e32 v[86:87], v[2:3]
	v_mov_b64_e32 v[88:89], v[2:3]
	v_mov_b64_e32 v[90:91], v[2:3]
	v_mov_b64_e32 v[92:93], v[2:3]
	v_mov_b64_e32 v[94:95], v[2:3]
	v_mov_b64_e32 v[96:97], v[2:3]
	v_mov_b64_e32 v[98:99], v[2:3]
	v_mov_b64_e32 v[100:101], v[2:3]
	v_mov_b64_e32 v[102:103], v[2:3]
	v_mov_b64_e32 v[104:105], v[2:3]
	v_mov_b64_e32 v[106:107], v[2:3]
	v_mov_b64_e32 v[108:109], v[2:3]
	v_mov_b64_e32 v[110:111], v[2:3]
	v_mov_b64_e32 v[112:113], v[2:3]
	v_mov_b64_e32 v[114:115], v[2:3]
	v_mov_b64_e32 v[116:117], v[2:3]
	v_mov_b64_e32 v[118:119], v[2:3]
	v_mov_b64_e32 v[120:121], v[2:3]
	v_mov_b64_e32 v[122:123], v[2:3]
	v_mov_b64_e32 v[124:125], v[2:3]
	v_mov_b64_e32 v[126:127], v[2:3]
	v_mov_b64_e32 v[128:129], v[2:3]
	.p2align	6

;     __device__ __forceinline__ bool next(int i, Unit& u) const { return unit_of((long)i * G + c, u); }
;     __device__ __forceinline__ bool next(int i, Unit& u) const { if (i >= 64) return false; return unit_of((long)__builtin_amdgcn_readfirstlane(list[i]), u); }
;     ...
;         const bool has_next = S.next(ui + 1, nxt);
;         const char* nA = has_next ? S.a_base(nxt) : cA; const char* nB = has_next ? S.b_base(nxt) : cB;
;         for (int t = 0; t < nt; t += 2) {
;             const bool last = (t == nt - 2);
;             const char* a1 = cA + (size_t)(t + 1) * kstep;
;             const char* a2 = last ? nA : cA + (size_t)(t + 2) * kstep; const char* b2 = last ? nB : cB + (size_t)(t + 2) * kstep;
;             const char* a3 = a2 + kstep; const char* b3 = b2 + kstep;
;     ...
;         for (int a = 0; a < 2; ++a)
; #pragma unroll
;             for (int b = 0; b < 2; ++b)
; #pragma unroll
;                 for (int m = 0; m < 4; ++m)
; #pragma unroll
;                     for (int n = 0; n < 2; ++n) acc[a][b][m][n] = (f32x4){0.f, 0.f, 0.f, 0.f};
;         cur = nxt; cA = nA; cB = nB; ++ui;
.LBB0_2270:
	s_ashr_i32 s75, s74, 31
	s_lshl_b64 s[0:1], s[74:75], 19
	s_add_u32 s0, s44, s0
	s_addc_u32 s1, s45, s1
	s_and_b64 s[16:17], s[46:47], exec
	s_cselect_b32 s15, s1, s93
	s_cselect_b32 s16, s0, s92
	s_add_u32 s92, s92, 0x40080
	v_lshl_add_u64 v[164:165], v[2:3], 0, s[88:89]
	v_mov_b32_e32 v2, 0
	s_addc_u32 s93, s93, 0
	s_mov_b32 s17, -2
	v_mov_b32_e32 v3, v2
	v_mov_b64_e32 v[4:5], v[2:3]
	v_mov_b64_e32 v[6:7], v[2:3]
	v_mov_b64_e32 v[8:9], v[2:3]
	v_mov_b64_e32 v[10:11], v[2:3]
	v_mov_b64_e32 v[12:13], v[2:3]
	v_mov_b64_e32 v[14:15], v[2:3]
	v_mov_b64_e32 v[16:17], v[2:3]
	v_mov_b64_e32 v[18:19], v[2:3]
	v_mov_b64_e32 v[20:21], v[2:3]
	v_mov_b64_e32 v[22:23], v[2:3]
	v_mov_b64_e32 v[24:25], v[2:3]
	v_mov_b64_e32 v[26:27], v[2:3]
	v_mov_b64_e32 v[28:29], v[2:3]
	v_mov_b64_e32 v[30:31], v[2:3]
	v_mov_b64_e32 v[32:33], v[2:3]
	v_mov_b64_e32 v[34:35], v[2:3]
	v_mov_b64_e32 v[36:37], v[2:3]
	v_mov_b64_e32 v[38:39], v[2:3]
	v_mov_b64_e32 v[40:41], v[2:3]
	v_mov_b64_e32 v[42:43], v[2:3]
	v_mov_b64_e32 v[44:45], v[2:3]
	v_mov_b64_e32 v[46:47], v[2:3]
	v_mov_b64_e32 v[48:49], v[2:3]
	v_mov_b64_e32 v[50:51], v[2:3]
	v_mov_b64_e32 v[52:53], v[2:3]
	v_mov_b64_e32 v[54:55], v[2:3]
	v_mov_b64_e32 v[56:57], v[2:3]
	v_mov_b64_e32 v[58:59], v[2:3]
	v_mov_b64_e32 v[60:61], v[2:3]
	v_mov_b64_e32 v[62:63], v[2:3]
	v_mov_b64_e32 v[64:65], v[2:3]
	v_mov_b64_e32 v[66:67], v[2:3]
	v_mov_b64_e32 v[68:69], v[2:3]
	v_mov_b64_e32 v[70:71], v[2:3]
	v_mov_b64_e32 v[72:73], v[2:3]
	v_mov_b64_e32 v[74:75], v[2:3]
	v_mov_b64_e32 v[76:77], v[2:3]
	v_mov_b64_e32 v[78:79], v[2:3]
	v_mov_b64_e32 v[80:81], v[2:3]
	v_mov_b64_e32 v[82:83], v[2:3]
	v_mov_b64_e32 v[84:85], v[2:3]
	v_mov_b64_e32 v[86:87], v[2:3]
	v_mov_b64_e32 v[88:89], v[2:3]
	v_mov_b64_e32 v[90:91], v[2:3]
	v_mov_b64_e32 v[92:93], v[2:3]
	v_mov_b64_e32 v[94:95], v[2:3]
	v_mov_b64_e32 v[96:97], v[2:3]
	v_mov_b64_e32 v[98:99], v[2:3]
	v_mov_b64_e32 v[100:101], v[2:3]
	v_mov_b64_e32 v[102:103], v[2:3]
	v_mov_b64_e32 v[104:105], v[2:3]
	v_mov_b64_e32 v[106:107], v[2:3]
	v_mov_b64_e32 v[108:109], v[2:3]
	v_mov_b64_e32 v[110:111], v[2:3]
	v_mov_b64_e32 v[112:113], v[2:3]
	v_mov_b64_e32 v[114:115], v[2:3]
	v_mov_b64_e32 v[116:117], v[2:3]
	v_mov_b64_e32 v[118:119], v[2:3]
	v_mov_b64_e32 v[120:121], v[2:3]
	v_mov_b64_e32 v[122:123], v[2:3]
	v_mov_b64_e32 v[124:125], v[2:3]
	v_mov_b64_e32 v[126:127], v[2:3]
	v_mov_b64_e32 v[128:129], v[2:3]
	.p2align	6

;     __device__ __forceinline__ bool next(int i, Unit& u) const { return unit_of((long)i * G + c, u); }
;     __device__ __forceinline__ bool next(int i, Unit& u) const { if (i >= 64) return false; return unit_of((long)__builtin_amdgcn_readfirstlane(list[i]), u); }
;     ...
;         const bool has_next = S.next(ui + 1, nxt);
;         const char* nA = has_next ? S.a_base(nxt) : cA; const char* nB = has_next ? S.b_base(nxt) : cB;
;         for (int t = 0; t < nt; t += 2) {
;             const bool last = (t == nt - 2);
;             const char* a1 = cA + (size_t)(t + 1) * kstep;
;             const char* a2 = last ? nA : cA + (size_t)(t + 2) * kstep; const char* b2 = last ? nB : cB + (size_t)(t + 2) * kstep;
;             const char* a3 = a2 + kstep; const char* b3 = b2 + kstep;
;     ...
;         for (int a = 0; a < 2; ++a)
; #pragma unroll
;             for (int b = 0; b < 2; ++b)
; #pragma unroll
;                 for (int m = 0; m < 4; ++m)
; #pragma unroll
;                     for (int n = 0; n < 2; ++n) acc[a][b][m][n] = (f32x4){0.f, 0.f, 0.f, 0.f};
;         cur = nxt; cA = nA; cB = nB; ++ui;
.LBB0_3093:
	s_ashr_i32 s11, s10, 31
	s_lshl_b64 s[12:13], s[10:11], 19
	s_add_u32 s12, s24, s12
	s_addc_u32 s13, s25, s13
	s_and_b64 s[14:15], s[4:5], exec
	s_cselect_b32 s11, s13, s19
	s_cselect_b32 s17, s12, s18
	s_ashr_i32 s9, s8, 31
	s_lshl_b64 s[14:15], s[8:9], 19
	s_add_u32 s14, s26, s14
	s_addc_u32 s15, s27, s15
	s_and_b64 s[22:23], s[4:5], exec
	s_cselect_b32 s9, s15, s21
	s_cselect_b32 s47, s14, s20
	s_add_u32 s18, s18, 0x40080
	s_addc_u32 s19, s19, 0
	s_add_u32 s50, s20, 0x100
	v_mov_b32_e32 v2, 0
	s_addc_u32 s51, s21, 0
	s_mov_b32 s52, -2
	v_mov_b32_e32 v3, v2
	v_mov_b32_e32 v4, v2
	v_mov_b32_e32 v5, v2
	v_mov_b32_e32 v6, v2
	v_mov_b32_e32 v7, v2
	v_mov_b32_e32 v8, v2
	v_mov_b32_e32 v9, v2
	v_mov_b32_e32 v14, v2
	v_mov_b32_e32 v15, v2
	v_mov_b32_e32 v16, v2
	v_mov_b32_e32 v17, v2
	v_mov_b32_e32 v22, v2
	v_mov_b32_e32 v23, v2
	v_mov_b32_e32 v24, v2
	v_mov_b32_e32 v25, v2
	v_mov_b32_e32 v30, v2
	v_mov_b32_e32 v31, v2
	v_mov_b32_e32 v32, v2
	v_mov_b32_e32 v33, v2
	v_mov_b32_e32 v38, v2
	v_mov_b32_e32 v39, v2
	v_mov_b32_e32 v40, v2
	v_mov_b32_e32 v41, v2
	v_mov_b32_e32 v46, v2
	v_mov_b32_e32 v47, v2
	v_mov_b32_e32 v48, v2
	v_mov_b32_e32 v49, v2
	v_mov_b32_e32 v54, v2
	v_mov_b32_e32 v55, v2
	v_mov_b32_e32 v56, v2
	v_mov_b32_e32 v57, v2
	v_mov_b32_e32 v10, v2
	v_mov_b32_e32 v11, v2
	v_mov_b32_e32 v12, v2
	v_mov_b32_e32 v13, v2
	v_mov_b32_e32 v18, v2
	v_mov_b32_e32 v19, v2
	v_mov_b32_e32 v20, v2
	v_mov_b32_e32 v21, v2
	v_mov_b32_e32 v26, v2
	v_mov_b32_e32 v27, v2
	v_mov_b32_e32 v28, v2
	v_mov_b32_e32 v29, v2
	v_mov_b32_e32 v34, v2
	v_mov_b32_e32 v35, v2
	v_mov_b32_e32 v36, v2
	v_mov_b32_e32 v37, v2
	v_mov_b32_e32 v42, v2
	v_mov_b32_e32 v43, v2
	v_mov_b32_e32 v44, v2
	v_mov_b32_e32 v45, v2
	v_mov_b32_e32 v50, v2
	v_mov_b32_e32 v51, v2
	v_mov_b32_e32 v52, v2
	v_mov_b32_e32 v53, v2
	v_mov_b32_e32 v58, v2
	v_mov_b32_e32 v59, v2
	v_mov_b32_e32 v60, v2
	v_mov_b32_e32 v61, v2
	v_mov_b32_e32 v62, v2
	v_mov_b32_e32 v63, v2
	v_mov_b32_e32 v64, v2
	v_mov_b32_e32 v65, v2
	v_mov_b32_e32 v66, v2
	v_mov_b32_e32 v67, v2
	v_mov_b32_e32 v68, v2
	v_mov_b32_e32 v69, v2
	v_mov_b32_e32 v70, v2
	v_mov_b32_e32 v71, v2
	v_mov_b32_e32 v72, v2
	v_mov_b32_e32 v73, v2
	v_mov_b32_e32 v78, v2
	v_mov_b32_e32 v79, v2
	v_mov_b32_e32 v80, v2
	v_mov_b32_e32 v81, v2
	v_mov_b32_e32 v86, v2
	v_mov_b32_e32 v87, v2
	v_mov_b32_e32 v88, v2
	v_mov_b32_e32 v89, v2
	v_mov_b32_e32 v94, v2
	v_mov_b32_e32 v95, v2
	v_mov_b32_e32 v96, v2
	v_mov_b32_e32 v97, v2
	v_mov_b32_e32 v102, v2
	v_mov_b32_e32 v103, v2
	v_mov_b32_e32 v104, v2
	v_mov_b32_e32 v105, v2
	v_mov_b32_e32 v130, v2
	v_mov_b32_e32 v131, v2
	v_mov_b32_e32 v132, v2
	v_mov_b32_e32 v133, v2
	v_mov_b32_e32 v134, v2
	v_mov_b32_e32 v135, v2
	v_mov_b32_e32 v136, v2
	v_mov_b32_e32 v137, v2
	v_mov_b32_e32 v74, v2
	v_mov_b32_e32 v75, v2
	v_mov_b32_e32 v76, v2
	v_mov_b32_e32 v77, v2
	v_mov_b32_e32 v82, v2
	v_mov_b32_e32 v83, v2
	v_mov_b32_e32 v84, v2
	v_mov_b32_e32 v85, v2
	v_mov_b32_e32 v90, v2
	v_mov_b32_e32 v91, v2
	v_mov_b32_e32 v92, v2
	v_mov_b32_e32 v93, v2
	v_mov_b32_e32 v98, v2
	v_mov_b32_e32 v99, v2
	v_mov_b32_e32 v100, v2
	v_mov_b32_e32 v101, v2
	v_mov_b32_e32 v106, v2
	v_mov_b32_e32 v107, v2
	v_mov_b32_e32 v108, v2
	v_mov_b32_e32 v109, v2
	v_mov_b32_e32 v110, v2
	v_mov_b32_e32 v111, v2
	v_mov_b32_e32 v112, v2
	v_mov_b32_e32 v113, v2
	v_mov_b32_e32 v138, v2
	v_mov_b32_e32 v139, v2
	v_mov_b32_e32 v140, v2
	v_mov_b32_e32 v141, v2
	v_mov_b32_e32 v142, v2
	v_mov_b32_e32 v143, v2
	v_mov_b32_e32 v144, v2
	v_mov_b32_e32 v145, v2
	.p2align	6

;     __device__ __forceinline__ bool next(int i, Unit& u) const { return unit_of((long)i * G + c, u); }
;     __device__ __forceinline__ bool next(int i, Unit& u) const { if (i >= 64) return false; return unit_of((long)__builtin_amdgcn_readfirstlane(list[i]), u); }
;     ...
;         const bool has_next = S.next(ui + 1, nxt);
;         const char* nA = has_next ? S.a_base(nxt) : cA; const char* nB = has_next ? S.b_base(nxt) : cB;
;         for (int t = 0; t < nt; t += 2) {
;             const bool last = (t == nt - 2);
;             const char* a1 = cA + (size_t)(t + 1) * kstep;
;             const char* a2 = last ? nA : cA + (size_t)(t + 2) * kstep; const char* b2 = last ? nB : cB + (size_t)(t + 2) * kstep;
;             const char* a3 = a2 + kstep; const char* b3 = b2 + kstep;
;     ...
;         for (int a = 0; a < 2; ++a)
; #pragma unroll
;             for (int b = 0; b < 2; ++b)
; #pragma unroll
;                 for (int m = 0; m < 4; ++m)
; #pragma unroll
;                     for (int n = 0; n < 2; ++n) acc[a][b][m][n] = (f32x4){0.f, 0.f, 0.f, 0.f};
;         cur = nxt; cA = nA; cB = nB; ++ui;
.LBB0_3247:
	s_ashr_i32 s13, s12, 31
	s_lshl_b64 s[14:15], s[12:13], 19
	s_add_u32 s14, s26, s14
	s_addc_u32 s15, s27, s15
	s_and_b64 s[16:17], s[4:5], exec
	s_cselect_b32 s13, s15, s21
	s_cselect_b32 s51, s14, s20
	s_ashr_i32 s11, s10, 31
	s_lshl_b64 s[16:17], s[10:11], 19
	s_add_u32 s16, s28, s16
	s_addc_u32 s17, s29, s17
	s_and_b64 s[24:25], s[4:5], exec
	s_cselect_b32 s11, s17, s23
	s_cselect_b32 s52, s16, s22
	s_add_u32 s20, s20, 0x40080
	s_addc_u32 s21, s21, 0
	s_add_u32 s53, s22, 0x100
	v_mov_b32_e32 v2, 0
	s_addc_u32 s54, s23, 0
	s_mov_b32 s55, -2
	v_mov_b32_e32 v3, v2
	v_mov_b64_e32 v[4:5], v[2:3]
	v_mov_b64_e32 v[6:7], v[2:3]
	v_mov_b64_e32 v[8:9], v[2:3]
	v_mov_b64_e32 v[10:11], v[2:3]
	v_mov_b64_e32 v[12:13], v[2:3]
	v_mov_b64_e32 v[14:15], v[2:3]
	v_mov_b64_e32 v[16:17], v[2:3]
	v_mov_b64_e32 v[18:19], v[2:3]
	v_mov_b64_e32 v[20:21], v[2:3]
	v_mov_b64_e32 v[22:23], v[2:3]
	v_mov_b64_e32 v[24:25], v[2:3]
	v_mov_b64_e32 v[26:27], v[2:3]
	v_mov_b64_e32 v[28:29], v[2:3]
	v_mov_b64_e32 v[30:31], v[2:3]
	v_mov_b64_e32 v[32:33], v[2:3]
	v_mov_b64_e32 v[34:35], v[2:3]
	v_mov_b64_e32 v[36:37], v[2:3]
	v_mov_b64_e32 v[38:39], v[2:3]
	v_mov_b64_e32 v[40:41], v[2:3]
	v_mov_b64_e32 v[42:43], v[2:3]
	v_mov_b64_e32 v[44:45], v[2:3]
	v_mov_b64_e32 v[46:47], v[2:3]
	v_mov_b64_e32 v[48:49], v[2:3]
	v_mov_b64_e32 v[50:51], v[2:3]
	v_mov_b64_e32 v[52:53], v[2:3]
	v_mov_b64_e32 v[54:55], v[2:3]
	v_mov_b64_e32 v[56:57], v[2:3]
	v_mov_b64_e32 v[58:59], v[2:3]
	v_mov_b64_e32 v[60:61], v[2:3]
	v_mov_b64_e32 v[62:63], v[2:3]
	v_mov_b64_e32 v[64:65], v[2:3]
	v_mov_b64_e32 v[66:67], v[2:3]
	v_mov_b64_e32 v[68:69], v[2:3]
	v_mov_b64_e32 v[70:71], v[2:3]
	v_mov_b64_e32 v[72:73], v[2:3]
	v_mov_b64_e32 v[74:75], v[2:3]
	v_mov_b64_e32 v[76:77], v[2:3]
	v_mov_b64_e32 v[78:79], v[2:3]
	v_mov_b64_e32 v[80:81], v[2:3]
	v_mov_b64_e32 v[82:83], v[2:3]
	v_mov_b64_e32 v[84:85], v[2:3]
	v_mov_b64_e32 v[86:87], v[2:3]
	v_mov_b64_e32 v[88:89], v[2:3]
	v_mov_b64_e32 v[90:91], v[2:3]
	v_mov_b64_e32 v[92:93], v[2:3]
	v_mov_b64_e32 v[94:95], v[2:3]
	v_mov_b64_e32 v[96:97], v[2:3]
	v_mov_b64_e32 v[98:99], v[2:3]
	v_mov_b64_e32 v[100:101], v[2:3]
	v_mov_b64_e32 v[102:103], v[2:3]
	v_mov_b64_e32 v[104:105], v[2:3]
	v_mov_b64_e32 v[106:107], v[2:3]
	v_mov_b64_e32 v[108:109], v[2:3]
	v_mov_b64_e32 v[110:111], v[2:3]
	v_mov_b64_e32 v[112:113], v[2:3]
	v_mov_b64_e32 v[114:115], v[2:3]
	v_mov_b64_e32 v[116:117], v[2:3]
	v_mov_b64_e32 v[118:119], v[2:3]
	v_mov_b64_e32 v[120:121], v[2:3]
	v_mov_b64_e32 v[122:123], v[2:3]
	v_mov_b64_e32 v[124:125], v[2:3]
	v_mov_b64_e32 v[126:127], v[2:3]
	v_mov_b64_e32 v[128:129], v[2:3]
	.p2align	6

;     ...
;             const char* a1 = cA + (size_t)(t + 1) * kstep;
;             const char* a2 = last ? nA : cA + (size_t)(t + 2) * kstep; const char* b2 = last ? nB : cB + (size_t)(t + 2) * kstep;
;             const char* a3 = a2 + kstep; const char* b3 = b2 + kstep;
;     ...
;         for (int a = 0; a < 2; ++a)
; #pragma unroll
;             for (int b = 0; b < 2; ++b)
; #pragma unroll
;                 for (int m = 0; m < 4; ++m)
; #pragma unroll
;                     for (int n = 0; n < 2; ++n) acc[a][b][m][n] = (f32x4){0.f, 0.f, 0.f, 0.f};
;         cur = nxt; cA = nA; cB = nB; ++ui;
.LBB0_3341:
	s_add_u32 s14, s14, 0xb0080
	s_addc_u32 s15, s15, 0
	s_add_u32 s13, s16, 0x100
	v_mov_b32_e32 v2, 0
	s_addc_u32 s44, s17, 0
	s_mov_b32 s45, -2
	v_mov_b32_e32 v3, v2
	v_mov_b32_e32 v4, v2
	v_mov_b32_e32 v5, v2
	v_mov_b32_e32 v6, v2
	v_mov_b32_e32 v7, v2
	v_mov_b32_e32 v8, v2
	v_mov_b32_e32 v9, v2
	v_mov_b32_e32 v14, v2
	v_mov_b32_e32 v15, v2
	v_mov_b32_e32 v16, v2
	v_mov_b32_e32 v17, v2
	v_mov_b32_e32 v22, v2
	v_mov_b32_e32 v23, v2
	v_mov_b32_e32 v24, v2
	v_mov_b32_e32 v25, v2
	v_mov_b32_e32 v30, v2
	v_mov_b32_e32 v31, v2
	v_mov_b32_e32 v32, v2
	v_mov_b32_e32 v33, v2
	v_mov_b32_e32 v38, v2
	v_mov_b32_e32 v39, v2
	v_mov_b32_e32 v40, v2
	v_mov_b32_e32 v41, v2
	v_mov_b32_e32 v46, v2
	v_mov_b32_e32 v47, v2
	v_mov_b32_e32 v48, v2
	v_mov_b32_e32 v49, v2
	v_mov_b32_e32 v54, v2
	v_mov_b32_e32 v55, v2
	v_mov_b32_e32 v56, v2
	v_mov_b32_e32 v57, v2
	v_mov_b32_e32 v10, v2
	v_mov_b32_e32 v11, v2
	v_mov_b32_e32 v12, v2
	v_mov_b32_e32 v13, v2
	v_mov_b32_e32 v18, v2
	v_mov_b32_e32 v19, v2
	v_mov_b32_e32 v20, v2
	v_mov_b32_e32 v21, v2
	v_mov_b32_e32 v26, v2
	v_mov_b32_e32 v27, v2
	v_mov_b32_e32 v28, v2
	v_mov_b32_e32 v29, v2
	v_mov_b32_e32 v34, v2
	v_mov_b32_e32 v35, v2
	v_mov_b32_e32 v36, v2
	v_mov_b32_e32 v37, v2
	v_mov_b32_e32 v42, v2
	v_mov_b32_e32 v43, v2
	v_mov_b32_e32 v44, v2
	v_mov_b32_e32 v45, v2
	v_mov_b32_e32 v50, v2
	v_mov_b32_e32 v51, v2
	v_mov_b32_e32 v52, v2
	v_mov_b32_e32 v53, v2
	v_mov_b32_e32 v58, v2
	v_mov_b32_e32 v59, v2
	v_mov_b32_e32 v60, v2
	v_mov_b32_e32 v61, v2
	v_mov_b32_e32 v62, v2
	v_mov_b32_e32 v63, v2
	v_mov_b32_e32 v64, v2
	v_mov_b32_e32 v65, v2
	v_mov_b32_e32 v66, v2
	v_mov_b32_e32 v67, v2
	v_mov_b32_e32 v68, v2
	v_mov_b32_e32 v69, v2
	v_mov_b32_e32 v70, v2
	v_mov_b32_e32 v71, v2
	v_mov_b32_e32 v72, v2
	v_mov_b32_e32 v73, v2
	v_mov_b32_e32 v78, v2
	v_mov_b32_e32 v79, v2
	v_mov_b32_e32 v80, v2
	v_mov_b32_e32 v81, v2
	v_mov_b32_e32 v86, v2
	v_mov_b32_e32 v87, v2
	v_mov_b32_e32 v88, v2
	v_mov_b32_e32 v89, v2
	v_mov_b32_e32 v94, v2
	v_mov_b32_e32 v95, v2
	v_mov_b32_e32 v96, v2
	v_mov_b32_e32 v97, v2
	v_mov_b32_e32 v102, v2
	v_mov_b32_e32 v103, v2
	v_mov_b32_e32 v104, v2
	v_mov_b32_e32 v105, v2
	v_mov_b32_e32 v130, v2
	v_mov_b32_e32 v131, v2
	v_mov_b32_e32 v132, v2
	v_mov_b32_e32 v133, v2
	v_mov_b32_e32 v134, v2
	v_mov_b32_e32 v135, v2
	v_mov_b32_e32 v136, v2
	v_mov_b32_e32 v137, v2
	v_mov_b32_e32 v74, v2
	v_mov_b32_e32 v75, v2
	v_mov_b32_e32 v76, v2
	v_mov_b32_e32 v77, v2
	v_mov_b32_e32 v82, v2
	v_mov_b32_e32 v83, v2
	v_mov_b32_e32 v84, v2
	v_mov_b32_e32 v85, v2
	v_mov_b32_e32 v90, v2
	v_mov_b32_e32 v91, v2
	v_mov_b32_e32 v92, v2
	v_mov_b32_e32 v93, v2
	v_mov_b32_e32 v98, v2
	v_mov_b32_e32 v99, v2
	v_mov_b32_e32 v100, v2
	v_mov_b32_e32 v101, v2
	v_mov_b32_e32 v106, v2
	v_mov_b32_e32 v107, v2
	v_mov_b32_e32 v108, v2
	v_mov_b32_e32 v109, v2
	v_mov_b32_e32 v110, v2
	v_mov_b32_e32 v111, v2
	v_mov_b32_e32 v112, v2
	v_mov_b32_e32 v113, v2
	v_mov_b32_e32 v138, v2
	v_mov_b32_e32 v139, v2
	v_mov_b32_e32 v140, v2
	v_mov_b32_e32 v141, v2
	v_mov_b32_e32 v142, v2
	v_mov_b32_e32 v143, v2
	v_mov_b32_e32 v144, v2
	v_mov_b32_e32 v145, v2
	.p2align	6

;     ...
;             const char* a1 = cA + (size_t)(t + 1) * kstep;
;             const char* a2 = last ? nA : cA + (size_t)(t + 2) * kstep; const char* b2 = last ? nB : cB + (size_t)(t + 2) * kstep;
;             const char* a3 = a2 + kstep; const char* b3 = b2 + kstep;
;     ...
;         for (int a = 0; a < 2; ++a)
; #pragma unroll
;             for (int b = 0; b < 2; ++b)
; #pragma unroll
;                 for (int m = 0; m < 4; ++m)
; #pragma unroll
;                     for (int n = 0; n < 2; ++n) acc[a][b][m][n] = (f32x4){0.f, 0.f, 0.f, 0.f};
;         cur = nxt; cA = nA; cB = nB; ++ui;
.LBB0_3369:
	s_add_u32 s14, s14, 0xb0080
	s_addc_u32 s15, s15, 0
	s_add_u32 s0, s16, 0x100
	v_mov_b32_e32 v2, 0
	s_addc_u32 s45, s17, 0
	s_mov_b32 s46, -2
	v_mov_b32_e32 v3, v2
	v_mov_b64_e32 v[4:5], v[2:3]
	v_mov_b64_e32 v[6:7], v[2:3]
	v_mov_b64_e32 v[8:9], v[2:3]
	v_mov_b64_e32 v[10:11], v[2:3]
	v_mov_b64_e32 v[12:13], v[2:3]
	v_mov_b64_e32 v[14:15], v[2:3]
	v_mov_b64_e32 v[16:17], v[2:3]
	v_mov_b64_e32 v[18:19], v[2:3]
	v_mov_b64_e32 v[20:21], v[2:3]
	v_mov_b64_e32 v[22:23], v[2:3]
	v_mov_b64_e32 v[24:25], v[2:3]
	v_mov_b64_e32 v[26:27], v[2:3]
	v_mov_b64_e32 v[28:29], v[2:3]
	v_mov_b64_e32 v[30:31], v[2:3]
	v_mov_b64_e32 v[32:33], v[2:3]
	v_mov_b64_e32 v[34:35], v[2:3]
	v_mov_b64_e32 v[36:37], v[2:3]
	v_mov_b64_e32 v[38:39], v[2:3]
	v_mov_b64_e32 v[40:41], v[2:3]
	v_mov_b64_e32 v[42:43], v[2:3]
	v_mov_b64_e32 v[44:45], v[2:3]
	v_mov_b64_e32 v[46:47], v[2:3]
	v_mov_b64_e32 v[48:49], v[2:3]
	v_mov_b64_e32 v[50:51], v[2:3]
	v_mov_b64_e32 v[52:53], v[2:3]
	v_mov_b64_e32 v[54:55], v[2:3]
	v_mov_b64_e32 v[56:57], v[2:3]
	v_mov_b64_e32 v[58:59], v[2:3]
	v_mov_b64_e32 v[60:61], v[2:3]
	v_mov_b64_e32 v[62:63], v[2:3]
	v_mov_b64_e32 v[64:65], v[2:3]
	v_mov_b64_e32 v[66:67], v[2:3]
	v_mov_b64_e32 v[68:69], v[2:3]
	v_mov_b64_e32 v[70:71], v[2:3]
	v_mov_b64_e32 v[72:73], v[2:3]
	v_mov_b64_e32 v[74:75], v[2:3]
	v_mov_b64_e32 v[76:77], v[2:3]
	v_mov_b64_e32 v[78:79], v[2:3]
	v_mov_b64_e32 v[80:81], v[2:3]
	v_mov_b64_e32 v[82:83], v[2:3]
	v_mov_b64_e32 v[84:85], v[2:3]
	v_mov_b64_e32 v[86:87], v[2:3]
	v_mov_b64_e32 v[88:89], v[2:3]
	v_mov_b64_e32 v[90:91], v[2:3]
	v_mov_b64_e32 v[92:93], v[2:3]
	v_mov_b64_e32 v[94:95], v[2:3]
	v_mov_b64_e32 v[96:97], v[2:3]
	v_mov_b64_e32 v[98:99], v[2:3]
	v_mov_b64_e32 v[100:101], v[2:3]
	v_mov_b64_e32 v[102:103], v[2:3]
	v_mov_b64_e32 v[104:105], v[2:3]
	v_mov_b64_e32 v[106:107], v[2:3]
	v_mov_b64_e32 v[108:109], v[2:3]
	v_mov_b64_e32 v[110:111], v[2:3]
	v_mov_b64_e32 v[112:113], v[2:3]
	v_mov_b64_e32 v[114:115], v[2:3]
	v_mov_b64_e32 v[116:117], v[2:3]
	v_mov_b64_e32 v[118:119], v[2:3]
	v_mov_b64_e32 v[120:121], v[2:3]
	v_mov_b64_e32 v[122:123], v[2:3]
	v_mov_b64_e32 v[124:125], v[2:3]
	v_mov_b64_e32 v[126:127], v[2:3]
	v_mov_b64_e32 v[128:129], v[2:3]
	.p2align	6

;     ...
;         for (int a = 0; a < 2; ++a)
; #pragma unroll
;             for (int b = 0; b < 2; ++b)
; #pragma unroll
;                 for (int m = 0; m < 4; ++m)
; #pragma unroll
;                     for (int n = 0; n < 2; ++n) acc[a][b][m][n] = (f32x4){0.f, 0.f, 0.f, 0.f};
;         cur = nxt; cA = nA; cB = nB; ++ui;
.LBB0_3555:
	s_ashr_i32 s17, s16, 31
	s_lshl_b64 s[20:21], s[16:17], 19
	s_cmpk_gt_i32 s14, 0x3e7
	s_cselect_b32 s15, s28, s30
	s_cselect_b32 s0, s29, s31
	s_add_u32 s20, s15, s20
	s_addc_u32 s21, s0, s21
	s_and_b64 s[26:27], s[26:27], exec
	s_cselect_b32 s0, s21, s25
	s_cselect_b32 s15, s20, s24
	s_add_u32 s22, s22, 0x40080
	s_addc_u32 s23, s23, 0
	s_add_u32 s17, s24, 0x100
	v_mov_b32_e32 v2, 0
	s_addc_u32 s47, s25, 0
	s_mov_b32 s48, -2
	v_mov_b32_e32 v3, v2
	v_mov_b64_e32 v[4:5], v[2:3]
	v_mov_b64_e32 v[6:7], v[2:3]
	v_mov_b64_e32 v[8:9], v[2:3]
	v_mov_b64_e32 v[10:11], v[2:3]
	v_mov_b64_e32 v[12:13], v[2:3]
	v_mov_b64_e32 v[14:15], v[2:3]
	v_mov_b64_e32 v[16:17], v[2:3]
	v_mov_b64_e32 v[18:19], v[2:3]
	v_mov_b64_e32 v[20:21], v[2:3]
	v_mov_b64_e32 v[22:23], v[2:3]
	v_mov_b64_e32 v[24:25], v[2:3]
	v_mov_b64_e32 v[26:27], v[2:3]
	v_mov_b64_e32 v[28:29], v[2:3]
	v_mov_b64_e32 v[30:31], v[2:3]
	v_mov_b64_e32 v[32:33], v[2:3]
	v_mov_b64_e32 v[34:35], v[2:3]
	v_mov_b64_e32 v[36:37], v[2:3]
	v_mov_b64_e32 v[38:39], v[2:3]
	v_mov_b64_e32 v[40:41], v[2:3]
	v_mov_b64_e32 v[42:43], v[2:3]
	v_mov_b64_e32 v[44:45], v[2:3]
	v_mov_b64_e32 v[46:47], v[2:3]
	v_mov_b64_e32 v[48:49], v[2:3]
	v_mov_b64_e32 v[50:51], v[2:3]
	v_mov_b64_e32 v[52:53], v[2:3]
	v_mov_b64_e32 v[54:55], v[2:3]
	v_mov_b64_e32 v[56:57], v[2:3]
	v_mov_b64_e32 v[58:59], v[2:3]
	v_mov_b64_e32 v[60:61], v[2:3]
	v_mov_b64_e32 v[62:63], v[2:3]
	v_mov_b64_e32 v[64:65], v[2:3]
	v_mov_b64_e32 v[66:67], v[2:3]
	v_mov_b64_e32 v[68:69], v[2:3]
	v_mov_b64_e32 v[70:71], v[2:3]
	v_mov_b64_e32 v[72:73], v[2:3]
	v_mov_b64_e32 v[74:75], v[2:3]
	v_mov_b64_e32 v[76:77], v[2:3]
	v_mov_b64_e32 v[78:79], v[2:3]
	v_mov_b64_e32 v[80:81], v[2:3]
	v_mov_b64_e32 v[82:83], v[2:3]
	v_mov_b64_e32 v[84:85], v[2:3]
	v_mov_b64_e32 v[86:87], v[2:3]
	v_mov_b64_e32 v[88:89], v[2:3]
	v_mov_b64_e32 v[90:91], v[2:3]
	v_mov_b64_e32 v[92:93], v[2:3]
	v_mov_b64_e32 v[94:95], v[2:3]
	v_mov_b64_e32 v[96:97], v[2:3]
	v_mov_b64_e32 v[98:99], v[2:3]
	v_mov_b64_e32 v[100:101], v[2:3]
	v_mov_b64_e32 v[102:103], v[2:3]
	v_mov_b64_e32 v[104:105], v[2:3]
	v_mov_b64_e32 v[106:107], v[2:3]
	v_mov_b64_e32 v[108:109], v[2:3]
	v_mov_b64_e32 v[110:111], v[2:3]
	v_mov_b64_e32 v[112:113], v[2:3]
	v_mov_b64_e32 v[114:115], v[2:3]
	v_mov_b64_e32 v[116:117], v[2:3]
	v_mov_b64_e32 v[118:119], v[2:3]
	v_mov_b64_e32 v[120:121], v[2:3]
	v_mov_b64_e32 v[122:123], v[2:3]
	v_mov_b64_e32 v[124:125], v[2:3]
	v_mov_b64_e32 v[126:127], v[2:3]
	v_mov_b64_e32 v[128:129], v[2:3]
	.p2align	6

;     __device__ __forceinline__ bool next(int i, Unit& u) const { return unit_of((long)i * G + c, u); }
;     __device__ __forceinline__ bool next(int i, Unit& u) const { if (i >= 64) return false; return unit_of((long)__builtin_amdgcn_readfirstlane(list[i]), u); }
;     ...
;         const bool has_next = S.next(ui + 1, nxt);
;         const char* nA = has_next ? S.a_base(nxt) : cA; const char* nB = has_next ? S.b_base(nxt) : cB;
;         for (int t = 0; t < nt; t += 2) {
;             const bool last = (t == nt - 2);
;             const char* a1 = cA + (size_t)(t + 1) * kstep;
;             const char* a2 = last ? nA : cA + (size_t)(t + 2) * kstep; const char* b2 = last ? nB : cB + (size_t)(t + 2) * kstep;
;             const char* a3 = a2 + kstep; const char* b3 = b2 + kstep;
;     ...
;         for (int a = 0; a < 2; ++a)
; #pragma unroll
;             for (int b = 0; b < 2; ++b)
; #pragma unroll
;                 for (int m = 0; m < 4; ++m)
; #pragma unroll
;                     for (int n = 0; n < 2; ++n) acc[a][b][m][n] = (f32x4){0.f, 0.f, 0.f, 0.f};
;         cur = nxt; cA = nA; cB = nB; ++ui;
.LBB0_4201:
	s_ashr_i32 s13, s12, 31
	s_lshl_b64 s[14:15], s[12:13], 19
	s_add_u32 s14, s27, s14
	s_addc_u32 s15, s28, s15
	s_and_b64 s[16:17], s[0:1], exec
	s_cselect_b32 s13, s15, s21
	s_cselect_b32 s19, s14, s20
	s_ashr_i32 s11, s10, 31
	s_lshl_b64 s[16:17], s[10:11], 19
	s_add_u32 s16, s29, s16
	s_addc_u32 s17, s30, s17
	s_and_b64 s[24:25], s[0:1], exec
	s_cselect_b32 s11, s17, s23
	s_cselect_b32 s49, s16, s22
	s_add_u32 s20, s20, 0x40080
	s_addc_u32 s21, s21, 0
	s_add_u32 s50, s22, 0x100
	v_mov_b32_e32 v2, 0
	s_addc_u32 s51, s23, 0
	s_mov_b32 s52, -2
	v_mov_b32_e32 v3, v2
	v_mov_b64_e32 v[4:5], v[2:3]
	v_mov_b64_e32 v[6:7], v[2:3]
	v_mov_b64_e32 v[8:9], v[2:3]
	v_mov_b64_e32 v[10:11], v[2:3]
	v_mov_b64_e32 v[12:13], v[2:3]
	v_mov_b64_e32 v[14:15], v[2:3]
	v_mov_b64_e32 v[16:17], v[2:3]
	v_mov_b64_e32 v[18:19], v[2:3]
	v_mov_b64_e32 v[20:21], v[2:3]
	v_mov_b64_e32 v[22:23], v[2:3]
	v_mov_b64_e32 v[24:25], v[2:3]
	v_mov_b64_e32 v[26:27], v[2:3]
	v_mov_b64_e32 v[28:29], v[2:3]
	v_mov_b64_e32 v[30:31], v[2:3]
	v_mov_b64_e32 v[32:33], v[2:3]
	v_mov_b64_e32 v[34:35], v[2:3]
	v_mov_b64_e32 v[36:37], v[2:3]
	v_mov_b64_e32 v[38:39], v[2:3]
	v_mov_b64_e32 v[40:41], v[2:3]
	v_mov_b64_e32 v[42:43], v[2:3]
	v_mov_b64_e32 v[44:45], v[2:3]
	v_mov_b64_e32 v[46:47], v[2:3]
	v_mov_b64_e32 v[48:49], v[2:3]
	v_mov_b64_e32 v[50:51], v[2:3]
	v_mov_b64_e32 v[52:53], v[2:3]
	v_mov_b64_e32 v[54:55], v[2:3]
	v_mov_b64_e32 v[56:57], v[2:3]
	v_mov_b64_e32 v[58:59], v[2:3]
	v_mov_b64_e32 v[60:61], v[2:3]
	v_mov_b64_e32 v[62:63], v[2:3]
	v_mov_b64_e32 v[64:65], v[2:3]
	v_mov_b64_e32 v[66:67], v[2:3]
	v_mov_b64_e32 v[68:69], v[2:3]
	v_mov_b64_e32 v[70:71], v[2:3]
	v_mov_b64_e32 v[72:73], v[2:3]
	v_mov_b64_e32 v[74:75], v[2:3]
	v_mov_b64_e32 v[76:77], v[2:3]
	v_mov_b64_e32 v[78:79], v[2:3]
	v_mov_b64_e32 v[80:81], v[2:3]
	v_mov_b64_e32 v[82:83], v[2:3]
	v_mov_b64_e32 v[84:85], v[2:3]
	v_mov_b64_e32 v[86:87], v[2:3]
	v_mov_b64_e32 v[88:89], v[2:3]
	v_mov_b64_e32 v[90:91], v[2:3]
	v_mov_b64_e32 v[92:93], v[2:3]
	v_mov_b64_e32 v[94:95], v[2:3]
	v_mov_b64_e32 v[96:97], v[2:3]
	v_mov_b64_e32 v[98:99], v[2:3]
	v_mov_b64_e32 v[100:101], v[2:3]
	v_mov_b64_e32 v[102:103], v[2:3]
	v_mov_b64_e32 v[104:105], v[2:3]
	v_mov_b64_e32 v[106:107], v[2:3]
	v_mov_b64_e32 v[108:109], v[2:3]
	v_mov_b64_e32 v[110:111], v[2:3]
	v_mov_b64_e32 v[112:113], v[2:3]
	v_mov_b64_e32 v[114:115], v[2:3]
	v_mov_b64_e32 v[116:117], v[2:3]
	v_mov_b64_e32 v[118:119], v[2:3]
	v_mov_b64_e32 v[120:121], v[2:3]
	v_mov_b64_e32 v[122:123], v[2:3]
	v_mov_b64_e32 v[124:125], v[2:3]
	v_mov_b64_e32 v[126:127], v[2:3]
	v_mov_b64_e32 v[128:129], v[2:3]
	.p2align	6

;     __device__ __forceinline__ bool next(int i, Unit& u) const { return unit_of((long)i * G + c, u); }
;     __device__ __forceinline__ bool next(int i, Unit& u) const { if (i >= 64) return false; return unit_of((long)__builtin_amdgcn_readfirstlane(list[i]), u); }
;     ...
;         const bool has_next = S.next(ui + 1, nxt);
;         const char* nA = has_next ? S.a_base(nxt) : cA; const char* nB = has_next ? S.b_base(nxt) : cB;
;         for (int t = 0; t < nt; t += 2) {
;             const bool last = (t == nt - 2);
;             const char* a1 = cA + (size_t)(t + 1) * kstep;
;             const char* a2 = last ? nA : cA + (size_t)(t + 2) * kstep; const char* b2 = last ? nB : cB + (size_t)(t + 2) * kstep;
;             const char* a3 = a2 + kstep; const char* b3 = b2 + kstep;
;     ...
;         for (int a = 0; a < 2; ++a)
; #pragma unroll
;             for (int b = 0; b < 2; ++b)
; #pragma unroll
;                 for (int m = 0; m < 4; ++m)
; #pragma unroll
;                     for (int n = 0; n < 2; ++n) acc[a][b][m][n] = (f32x4){0.f, 0.f, 0.f, 0.f};
;         cur = nxt; cA = nA; cB = nB; ++ui;
.LBB0_4504:
	s_add_u32 s50, s50, 0xe0080
	v_lshl_add_u64 v[164:165], v[2:3], 0, s[30:31]
	v_mov_b32_e32 v2, 0
	s_addc_u32 s51, s51, 0
	s_mov_b32 s83, -2
	v_mov_b32_e32 v3, v2
	v_mov_b64_e32 v[4:5], v[2:3]
	v_mov_b64_e32 v[6:7], v[2:3]
	v_mov_b64_e32 v[8:9], v[2:3]
	v_mov_b64_e32 v[10:11], v[2:3]
	v_mov_b64_e32 v[12:13], v[2:3]
	v_mov_b64_e32 v[14:15], v[2:3]
	v_mov_b64_e32 v[16:17], v[2:3]
	v_mov_b64_e32 v[18:19], v[2:3]
	v_mov_b64_e32 v[20:21], v[2:3]
	v_mov_b64_e32 v[22:23], v[2:3]
	v_mov_b64_e32 v[24:25], v[2:3]
	v_mov_b64_e32 v[26:27], v[2:3]
	v_mov_b64_e32 v[28:29], v[2:3]
	v_mov_b64_e32 v[30:31], v[2:3]
	v_mov_b64_e32 v[32:33], v[2:3]
	v_mov_b64_e32 v[34:35], v[2:3]
	v_mov_b64_e32 v[36:37], v[2:3]
	v_mov_b64_e32 v[38:39], v[2:3]
	v_mov_b64_e32 v[40:41], v[2:3]
	v_mov_b64_e32 v[42:43], v[2:3]
	v_mov_b64_e32 v[44:45], v[2:3]
	v_mov_b64_e32 v[46:47], v[2:3]
	v_mov_b64_e32 v[48:49], v[2:3]
	v_mov_b64_e32 v[50:51], v[2:3]
	v_mov_b64_e32 v[52:53], v[2:3]
	v_mov_b64_e32 v[54:55], v[2:3]
	v_mov_b64_e32 v[56:57], v[2:3]
	v_mov_b64_e32 v[58:59], v[2:3]
	v_mov_b64_e32 v[60:61], v[2:3]
	v_mov_b64_e32 v[62:63], v[2:3]
	v_mov_b64_e32 v[64:65], v[2:3]
	v_mov_b64_e32 v[66:67], v[2:3]
	v_mov_b64_e32 v[68:69], v[2:3]
	v_mov_b64_e32 v[70:71], v[2:3]
	v_mov_b64_e32 v[72:73], v[2:3]
	v_mov_b64_e32 v[74:75], v[2:3]
	v_mov_b64_e32 v[76:77], v[2:3]
	v_mov_b64_e32 v[78:79], v[2:3]
	v_mov_b64_e32 v[80:81], v[2:3]
	v_mov_b64_e32 v[82:83], v[2:3]
	v_mov_b64_e32 v[84:85], v[2:3]
	v_mov_b64_e32 v[86:87], v[2:3]
	v_mov_b64_e32 v[88:89], v[2:3]
	v_mov_b64_e32 v[90:91], v[2:3]
	v_mov_b64_e32 v[92:93], v[2:3]
	v_mov_b64_e32 v[94:95], v[2:3]
	v_mov_b64_e32 v[96:97], v[2:3]
	v_mov_b64_e32 v[98:99], v[2:3]
	v_mov_b64_e32 v[100:101], v[2:3]
	v_mov_b64_e32 v[102:103], v[2:3]
	v_mov_b64_e32 v[104:105], v[2:3]
	v_mov_b64_e32 v[106:107], v[2:3]
	v_mov_b64_e32 v[108:109], v[2:3]
	v_mov_b64_e32 v[110:111], v[2:3]
	v_mov_b64_e32 v[112:113], v[2:3]
	v_mov_b64_e32 v[114:115], v[2:3]
	v_mov_b64_e32 v[116:117], v[2:3]
	v_mov_b64_e32 v[118:119], v[2:3]
	v_mov_b64_e32 v[120:121], v[2:3]
	v_mov_b64_e32 v[122:123], v[2:3]
	v_mov_b64_e32 v[124:125], v[2:3]
	v_mov_b64_e32 v[126:127], v[2:3]
	v_mov_b64_e32 v[128:129], v[2:3]
	.p2align	6

;     __device__ __forceinline__ bool next(int i, Unit& u) const { return unit_of((long)i * G + c, u); }
;     __device__ __forceinline__ bool next(int i, Unit& u) const { if (i >= 64) return false; return unit_of((long)__builtin_amdgcn_readfirstlane(list[i]), u); }
;     ...
;         const bool has_next = S.next(ui + 1, nxt);
;         const char* nA = has_next ? S.a_base(nxt) : cA; const char* nB = has_next ? S.b_base(nxt) : cB;
;         for (int t = 0; t < nt; t += 2) {
;             const bool last = (t == nt - 2);
;             const char* a1 = cA + (size_t)(t + 1) * kstep;
;             const char* a2 = last ? nA : cA + (size_t)(t + 2) * kstep; const char* b2 = last ? nB : cB + (size_t)(t + 2) * kstep;
;             const char* a3 = a2 + kstep; const char* b3 = b2 + kstep;
;     ...
;         for (int a = 0; a < 2; ++a)
; #pragma unroll
;             for (int b = 0; b < 2; ++b)
; #pragma unroll
;                 for (int m = 0; m < 4; ++m)
; #pragma unroll
;                     for (int n = 0; n < 2; ++n) acc[a][b][m][n] = (f32x4){0.f, 0.f, 0.f, 0.f};
;         cur = nxt; cA = nA; cB = nB; ++ui;
.LBB0_4533:
	s_ashr_i32 s51, s50, 31
	s_lshl_b64 s[42:43], s[50:51], 19
	s_add_u32 s42, s72, s42
	s_addc_u32 s43, s73, s43
	s_and_b64 s[56:57], s[56:57], exec
	s_cselect_b32 s3, s43, s55
	s_cselect_b32 s51, s42, s54
	s_add_u32 s54, s54, 0x40080
	v_lshl_add_u64 v[164:165], v[2:3], 0, s[30:31]
	v_mov_b32_e32 v2, 0
	s_addc_u32 s55, s55, 0
	s_mov_b32 s80, -2
	v_mov_b32_e32 v3, v2
	v_mov_b64_e32 v[4:5], v[2:3]
	v_mov_b64_e32 v[6:7], v[2:3]
	v_mov_b64_e32 v[8:9], v[2:3]
	v_mov_b64_e32 v[10:11], v[2:3]
	v_mov_b64_e32 v[12:13], v[2:3]
	v_mov_b64_e32 v[14:15], v[2:3]
	v_mov_b64_e32 v[16:17], v[2:3]
	v_mov_b64_e32 v[18:19], v[2:3]
	v_mov_b64_e32 v[20:21], v[2:3]
	v_mov_b64_e32 v[22:23], v[2:3]
	v_mov_b64_e32 v[24:25], v[2:3]
	v_mov_b64_e32 v[26:27], v[2:3]
	v_mov_b64_e32 v[28:29], v[2:3]
	v_mov_b64_e32 v[30:31], v[2:3]
	v_mov_b64_e32 v[32:33], v[2:3]
	v_mov_b64_e32 v[34:35], v[2:3]
	v_mov_b64_e32 v[36:37], v[2:3]
	v_mov_b64_e32 v[38:39], v[2:3]
	v_mov_b64_e32 v[40:41], v[2:3]
	v_mov_b64_e32 v[42:43], v[2:3]
	v_mov_b64_e32 v[44:45], v[2:3]
	v_mov_b64_e32 v[46:47], v[2:3]
	v_mov_b64_e32 v[48:49], v[2:3]
	v_mov_b64_e32 v[50:51], v[2:3]
	v_mov_b64_e32 v[52:53], v[2:3]
	v_mov_b64_e32 v[54:55], v[2:3]
	v_mov_b64_e32 v[56:57], v[2:3]
	v_mov_b64_e32 v[58:59], v[2:3]
	v_mov_b64_e32 v[60:61], v[2:3]
	v_mov_b64_e32 v[62:63], v[2:3]
	v_mov_b64_e32 v[64:65], v[2:3]
	v_mov_b64_e32 v[66:67], v[2:3]
	v_mov_b64_e32 v[68:69], v[2:3]
	v_mov_b64_e32 v[70:71], v[2:3]
	v_mov_b64_e32 v[72:73], v[2:3]
	v_mov_b64_e32 v[74:75], v[2:3]
	v_mov_b64_e32 v[76:77], v[2:3]
	v_mov_b64_e32 v[78:79], v[2:3]
	v_mov_b64_e32 v[80:81], v[2:3]
	v_mov_b64_e32 v[82:83], v[2:3]
	v_mov_b64_e32 v[84:85], v[2:3]
	v_mov_b64_e32 v[86:87], v[2:3]
	v_mov_b64_e32 v[88:89], v[2:3]
	v_mov_b64_e32 v[90:91], v[2:3]
	v_mov_b64_e32 v[92:93], v[2:3]
	v_mov_b64_e32 v[94:95], v[2:3]
	v_mov_b64_e32 v[96:97], v[2:3]
	v_mov_b64_e32 v[98:99], v[2:3]
	v_mov_b64_e32 v[100:101], v[2:3]
	v_mov_b64_e32 v[102:103], v[2:3]
	v_mov_b64_e32 v[104:105], v[2:3]
	v_mov_b64_e32 v[106:107], v[2:3]
	v_mov_b64_e32 v[108:109], v[2:3]
	v_mov_b64_e32 v[110:111], v[2:3]
	v_mov_b64_e32 v[112:113], v[2:3]
	v_mov_b64_e32 v[114:115], v[2:3]
	v_mov_b64_e32 v[116:117], v[2:3]
	v_mov_b64_e32 v[118:119], v[2:3]
	v_mov_b64_e32 v[120:121], v[2:3]
	v_mov_b64_e32 v[122:123], v[2:3]
	v_mov_b64_e32 v[124:125], v[2:3]
	v_mov_b64_e32 v[126:127], v[2:3]
	v_mov_b64_e32 v[128:129], v[2:3]
	.p2align	6
